# s11 + attention row-sum as two interleaved partial sums (second in v245), merged by the chain's former +0 add
# speedup vs baseline: 1.0029x; 1.0029x over previous
; __device__ __forceinline__ void cmask(f32x16& p0, f32x16& p1, int jb, int qrel, int hi) {
;     const float NEG = -INFINITY; int kb = 64 * jb + 4 * hi;
; #pragma unroll
;     for (int r = 0; r < 16; ++r) { int kv = kb + (r & 3) + 8 * (r >> 2); if (kv > qrel) p0[r] = NEG; if (kv + 32 > qrel) p1[r] = NEG; }
; }
.LBB0_477:
	v_add_u32_e32 v184, s0, v230
	ds_read_b64_tr_b16 v[180:181], v184 offset:24576
	ds_read_b64_tr_b16 v[182:183], v184 offset:25088
	s_waitcnt lgkmcnt(9)
	v_mfma_f32_32x32x16_f16 v[48:63], v[176:179], v[128:131], v[48:63]
	v_add_f32_e32 v132, v80, v81
	v_add_f32_e32 v245, v82, v83
	v_add_f32_e32 v132, v84, v132
	v_add_f32_e32 v245, v85, v245
	v_cvt_pk_f16_f32 v144, v80, v81
	v_cvt_pk_f16_f32 v145, v82, v83
	ds_read_b64_tr_b16 v[176:177], v184 offset:28672
	ds_read_b64_tr_b16 v[178:179], v184 offset:29184
	s_waitcnt lgkmcnt(10)
	v_mfma_f32_32x32x16_f16 v[32:47], v[172:175], v[128:131], v[32:47]
	v_add_f32_e32 v80, v86, v132
	v_add_f32_e32 v245, v87, v245
	v_add_f32_e32 v80, v88, v80
	v_add_f32_e32 v245, v89, v245
	v_cvt_pk_f16_f32 v146, v84, v85
	v_cvt_pk_f16_f32 v147, v86, v87
	ds_read_b64_tr_b16 v[172:173], v184 offset:25600
	ds_read_b64_tr_b16 v[174:175], v184 offset:26112
	s_waitcnt lgkmcnt(11)
	v_mfma_f32_32x32x16_f16 v[48:63], v[168:171], v[124:127], v[48:63]
	v_add_f32_e32 v80, v90, v80
	v_add_f32_e32 v245, v91, v245
	v_add_f32_e32 v80, v92, v80
	v_add_f32_e32 v245, v93, v245
	v_cvt_pk_f16_f32 v140, v88, v89
	v_cvt_pk_f16_f32 v141, v90, v91
	ds_read_b64_tr_b16 v[84:85], v184 offset:29696
	ds_read_b64_tr_b16 v[86:87], v184 offset:30208
	s_waitcnt lgkmcnt(12)
	v_mfma_f32_32x32x16_f16 v[32:47], v[164:167], v[124:127], v[32:47]
	v_add_f32_e32 v80, v94, v80
	v_add_f32_e32 v245, v95, v245
	v_add_f32_e32 v80, v64, v80
	v_add_f32_e32 v88, v65, v80
	v_cvt_pk_f16_f32 v142, v92, v93
	v_cvt_pk_f16_f32 v143, v94, v95
	ds_read_b64_tr_b16 v[80:81], v184 offset:26624
	ds_read_b64_tr_b16 v[82:83], v184 offset:27136
	s_waitcnt lgkmcnt(13)
	v_mfma_f32_32x32x16_f16 v[48:63], v[160:163], v[120:123], v[48:63]
	v_add_f32_e32 v245, v66, v245
	v_add_f32_e32 v88, v67, v88
	v_add_f32_e32 v245, v68, v245
	v_add_f32_e32 v88, v69, v88
	v_cvt_pk_f16_f32 v136, v64, v65
	v_cvt_pk_f16_f32 v137, v66, v67
	ds_read_b64_tr_b16 v[160:161], v184 offset:30720
	ds_read_b64_tr_b16 v[162:163], v184 offset:31232
	s_waitcnt lgkmcnt(14)
	v_mfma_f32_32x32x16_f16 v[32:47], v[152:155], v[120:123], v[32:47]
	v_add_f32_e32 v64, v70, v88
	v_add_f32_e32 v245, v71, v245
	v_add_f32_e32 v64, v72, v64
	v_add_f32_e32 v88, v73, v64
	v_cvt_pk_f16_f32 v138, v68, v69
	v_cvt_pk_f16_f32 v139, v70, v71
	ds_read_b64_tr_b16 v[64:65], v184 offset:27648
	ds_read_b64_tr_b16 v[66:67], v184 offset:28160
	s_waitcnt lgkmcnt(14)
	v_mfma_f32_32x32x16_f16 v[48:63], v[156:159], v[116:119], v[48:63]
	v_add_f32_e32 v68, v74, v88
	v_add_f32_e32 v245, v75, v245
	v_add_f32_e32 v68, v76, v68
	v_add_f32_e32 v245, v77, v245
	v_cvt_pk_f16_f32 v132, v72, v73
	v_cvt_pk_f16_f32 v133, v74, v75
	ds_read_b64_tr_b16 v[152:153], v184 offset:31744
	ds_read_b64_tr_b16 v[154:155], v184 offset:32256
	v_mfma_f32_32x32x16_f16 v[32:47], v[148:151], v[116:119], v[32:47]
	v_add_f32_e32 v68, v78, v68
	v_add_f32_e32 v245, v79, v245
	v_add_f32_e32 v68, v245, v68
	v_cvt_pk_f16_f32 v134, v76, v77
	v_cvt_pk_f16_f32 v135, v78, v79
	s_add_i32 s0, s70, s89
	s_cmp_lt_u32 s69, 3
	s_cselect_b64 s[40:41], -1, 0
	s_mov_b32 s1, m0
	s_mov_b32 m0, s0
	s_nop 0
	global_load_lds_dwordx4 v[194:195], off
	s_mov_b32 m0, s1
	s_and_b64 s[0:1], s[40:41], exec
	s_cselect_b32 s18, s50, -3
	s_add_i32 s18, s18, s69
	v_mad_i64_i32 v[70:71], s[0:1], s18, v249, v[216:217]
	s_add_i32 s0, s68, s36
	s_mov_b32 s1, m0
	s_mov_b32 m0, s0
	s_nop 0
	global_load_lds_dwordx4 v[70:71], off
	s_mov_b32 m0, s1
	s_cmp_gt_u32 s69, 3
	s_cbranch_scc1 .LBB0_479
	s_mov_b64 s[100:101], exec
	v_sub_u32_e32 v70, v215, v197
	v_add_u32_e32 v70, 0x7b, v70
	v_cmpx_gt_i32_e32 59, v70
	s_nop 3
	s_cbranch_execz .Lmaskx_done_9
	v_mov_b32_e32 v47, v248
	v_cmpx_gt_i32_e32 58, v70
	v_mov_b32_e32 v46, v248
	v_cmpx_gt_i32_e32 57, v70
	v_mov_b32_e32 v45, v248
	v_cmpx_gt_i32_e32 56, v70
	v_mov_b32_e32 v44, v248
	v_cmpx_gt_i32_e32 51, v70
	v_mov_b32_e32 v43, v248
	v_cmpx_gt_i32_e32 50, v70
	v_mov_b32_e32 v42, v248
	v_cmpx_gt_i32_e32 49, v70
	v_mov_b32_e32 v41, v248
	v_cmpx_gt_i32_e32 48, v70
	v_mov_b32_e32 v40, v248
	v_cmpx_gt_i32_e32 43, v70
	v_mov_b32_e32 v39, v248
	v_cmpx_gt_i32_e32 42, v70
	v_mov_b32_e32 v38, v248
	v_cmpx_gt_i32_e32 41, v70
	v_mov_b32_e32 v37, v248
	v_cmpx_gt_i32_e32 40, v70
	v_mov_b32_e32 v36, v248
	v_cmpx_gt_i32_e32 35, v70
	v_mov_b32_e32 v35, v248
	v_cmpx_gt_i32_e32 34, v70
	v_mov_b32_e32 v34, v248
	v_cmpx_gt_i32_e32 33, v70
	v_mov_b32_e32 v33, v248
	v_cmpx_gt_i32_e32 32, v70
	v_mov_b32_e32 v32, v248
	v_cmpx_gt_i32_e32 27, v70
	v_mov_b32_e32 v63, v248
	v_cmpx_gt_i32_e32 26, v70
	v_mov_b32_e32 v62, v248
	v_cmpx_gt_i32_e32 25, v70
	v_mov_b32_e32 v61, v248
	v_cmpx_gt_i32_e32 24, v70
	v_mov_b32_e32 v60, v248
	v_cmpx_gt_i32_e32 19, v70
	v_mov_b32_e32 v59, v248
	v_cmpx_gt_i32_e32 18, v70
	v_mov_b32_e32 v58, v248
	v_cmpx_gt_i32_e32 17, v70
	v_mov_b32_e32 v57, v248
	v_cmpx_gt_i32_e32 16, v70
	v_mov_b32_e32 v56, v248
	v_cmpx_gt_i32_e32 11, v70
	v_mov_b32_e32 v55, v248
	v_cmpx_gt_i32_e32 10, v70
	v_mov_b32_e32 v54, v248
	v_cmpx_gt_i32_e32 9, v70
	v_mov_b32_e32 v53, v248
	v_cmpx_gt_i32_e32 8, v70
	v_mov_b32_e32 v52, v248
	v_cmpx_gt_i32_e32 3, v70
	v_mov_b32_e32 v51, v248
	v_cmpx_gt_i32_e32 2, v70
	v_mov_b32_e32 v50, v248
	v_cmpx_gt_i32_e32 1, v70
	v_mov_b32_e32 v49, v248
	v_cmpx_gt_i32_e32 0, v70
	v_mov_b32_e32 v48, v248

; __device__ __forceinline__ void cmask(f32x16& p0, f32x16& p1, int jb, int qrel, int hi) {
;     const float NEG = -INFINITY; int kb = 64 * jb + 4 * hi;
; #pragma unroll
;     for (int r = 0; r < 16; ++r) { int kv = kb + (r & 3) + 8 * (r >> 2); if (kv > qrel) p0[r] = NEG; if (kv + 32 > qrel) p1[r] = NEG; }
; }
.LBB0_482:
	s_add_i32 s0, s68, 0x2000
	s_cmpk_lg_i32 s68, 0x4000
	s_cselect_b32 s45, s0, 0
	v_add_u32_e32 v160, s70, v230
	ds_read_b64_tr_b16 v[156:157], v160 offset:24576
	ds_read_b64_tr_b16 v[158:159], v160 offset:25088
	v_mfma_f32_32x32x16_f16 v[80:95], v[188:191], v[128:131], v[80:95]
	v_add_f32_e32 v132, v48, v49
	v_add_f32_e32 v245, v50, v51
	v_add_f32_e32 v132, v52, v132
	v_add_f32_e32 v245, v53, v245
	v_cvt_pk_f16_f32 v144, v48, v49
	v_cvt_pk_f16_f32 v145, v50, v51
	ds_read_b64_tr_b16 v[152:153], v160 offset:28672
	ds_read_b64_tr_b16 v[154:155], v160 offset:29184
	v_mfma_f32_32x32x16_f16 v[64:79], v[148:151], v[128:131], v[64:79]
	v_add_f32_e32 v48, v54, v132
	v_add_f32_e32 v245, v55, v245
	v_add_f32_e32 v48, v56, v48
	v_add_f32_e32 v245, v57, v245
	v_cvt_pk_f16_f32 v146, v52, v53
	v_cvt_pk_f16_f32 v147, v54, v55
	ds_read_b64_tr_b16 v[148:149], v160 offset:25600
	ds_read_b64_tr_b16 v[150:151], v160 offset:26112
	v_mfma_f32_32x32x16_f16 v[80:95], v[184:187], v[124:127], v[80:95]
	v_add_f32_e32 v48, v58, v48
	v_add_f32_e32 v245, v59, v245
	v_add_f32_e32 v48, v60, v48
	v_add_f32_e32 v245, v61, v245
	v_cvt_pk_f16_f32 v140, v56, v57
	v_cvt_pk_f16_f32 v141, v58, v59
	ds_read_b64_tr_b16 v[52:53], v160 offset:29696
	ds_read_b64_tr_b16 v[54:55], v160 offset:30208
	v_mfma_f32_32x32x16_f16 v[64:79], v[172:175], v[124:127], v[64:79]
	v_add_f32_e32 v48, v62, v48
	v_add_f32_e32 v245, v63, v245
	v_add_f32_e32 v48, v32, v48
	v_add_f32_e32 v56, v33, v48
	v_cvt_pk_f16_f32 v142, v60, v61
	v_cvt_pk_f16_f32 v143, v62, v63
	ds_read_b64_tr_b16 v[48:49], v160 offset:26624
	ds_read_b64_tr_b16 v[50:51], v160 offset:27136
	s_waitcnt lgkmcnt(13)
	v_mfma_f32_32x32x16_f16 v[80:95], v[176:179], v[120:123], v[80:95]
	v_add_f32_e32 v245, v34, v245
	v_add_f32_e32 v56, v35, v56
	v_add_f32_e32 v245, v36, v245
	v_add_f32_e32 v56, v37, v56
	v_cvt_pk_f16_f32 v136, v32, v33
	v_cvt_pk_f16_f32 v137, v34, v35
	ds_read_b64_tr_b16 v[184:185], v160 offset:30720
	ds_read_b64_tr_b16 v[186:187], v160 offset:31232
	s_waitcnt lgkmcnt(14)
	v_mfma_f32_32x32x16_f16 v[64:79], v[164:167], v[120:123], v[64:79]
	v_add_f32_e32 v32, v38, v56
	v_add_f32_e32 v245, v39, v245
	v_add_f32_e32 v32, v40, v32
	v_add_f32_e32 v56, v41, v32
	v_cvt_pk_f16_f32 v138, v36, v37
	v_cvt_pk_f16_f32 v139, v38, v39
	ds_read_b64_tr_b16 v[32:33], v160 offset:27648
	ds_read_b64_tr_b16 v[34:35], v160 offset:28160
	s_waitcnt lgkmcnt(14)
	v_mfma_f32_32x32x16_f16 v[80:95], v[180:183], v[116:119], v[80:95]
	v_add_f32_e32 v36, v42, v56
	v_add_f32_e32 v245, v43, v245
	v_add_f32_e32 v36, v44, v36
	v_add_f32_e32 v245, v45, v245
	v_cvt_pk_f16_f32 v132, v40, v41
	v_cvt_pk_f16_f32 v133, v42, v43
	ds_read_b64_tr_b16 v[180:181], v160 offset:31744
	ds_read_b64_tr_b16 v[182:183], v160 offset:32256
	v_mfma_f32_32x32x16_f16 v[64:79], v[168:171], v[116:119], v[64:79]
	v_add_f32_e32 v36, v46, v36
	v_add_f32_e32 v245, v47, v245
	v_add_f32_e32 v36, v245, v36
	v_cvt_pk_f16_f32 v134, v44, v45
	v_cvt_pk_f16_f32 v135, v46, v47
	s_add_i32 s0, s68, s89
	v_lshl_add_u64 v[38:39], v[194:195], 0, s[30:31]
	s_mov_b32 s1, m0
	s_mov_b32 m0, s0
	s_nop 0
	global_load_lds_dwordx4 v[38:39], off
	s_mov_b32 m0, s1
	s_cmp_lt_u32 s69, 2
	s_cselect_b64 s[0:1], -1, 0
	s_and_b64 s[18:19], s[0:1], exec
	s_cselect_b32 s18, s51, -2
	s_add_i32 s18, s18, s69
	v_mad_i64_i32 v[38:39], s[46:47], s18, v249, v[216:217]
	s_add_i32 s19, s45, s36
	s_mov_b32 s46, m0
	s_mov_b32 m0, s19
	s_nop 0
	global_load_lds_dwordx4 v[38:39], off
	s_mov_b32 m0, s46
	s_andn2_b64 vcc, exec, s[40:41]
	s_cbranch_vccnz .LBB0_484
	s_mov_b64 s[100:101], exec
	v_sub_u32_e32 v38, v215, v197
	v_add_u32_e32 v38, 59, v38
	v_cmpx_gt_i32_e32 59, v38
	s_nop 3
	s_cbranch_execz .Lmaskx_done_8
	v_mov_b32_e32 v79, v248
	v_cmpx_gt_i32_e32 58, v38
	v_mov_b32_e32 v78, v248
	v_cmpx_gt_i32_e32 57, v38
	v_mov_b32_e32 v77, v248
	v_cmpx_gt_i32_e32 56, v38
	v_mov_b32_e32 v76, v248
	v_cmpx_gt_i32_e32 51, v38
	v_mov_b32_e32 v75, v248
	v_cmpx_gt_i32_e32 50, v38
	v_mov_b32_e32 v74, v248
	v_cmpx_gt_i32_e32 49, v38
	v_mov_b32_e32 v73, v248
	v_cmpx_gt_i32_e32 48, v38
	v_mov_b32_e32 v72, v248
	v_cmpx_gt_i32_e32 43, v38
	v_mov_b32_e32 v71, v248
	v_cmpx_gt_i32_e32 42, v38
	v_mov_b32_e32 v70, v248
	v_cmpx_gt_i32_e32 41, v38
	v_mov_b32_e32 v69, v248
	v_cmpx_gt_i32_e32 40, v38
	v_mov_b32_e32 v68, v248
	v_cmpx_gt_i32_e32 35, v38
	v_mov_b32_e32 v67, v248
	v_cmpx_gt_i32_e32 34, v38
	v_mov_b32_e32 v66, v248
	v_cmpx_gt_i32_e32 33, v38
	v_mov_b32_e32 v65, v248
	v_cmpx_gt_i32_e32 32, v38
	v_mov_b32_e32 v64, v248
	v_cmpx_gt_i32_e32 27, v38
	v_mov_b32_e32 v95, v248
	v_cmpx_gt_i32_e32 26, v38
	v_mov_b32_e32 v94, v248
	v_cmpx_gt_i32_e32 25, v38
	v_mov_b32_e32 v93, v248
	v_cmpx_gt_i32_e32 24, v38
	v_mov_b32_e32 v92, v248
	v_cmpx_gt_i32_e32 19, v38
	v_mov_b32_e32 v91, v248
	v_cmpx_gt_i32_e32 18, v38
	v_mov_b32_e32 v90, v248
	v_cmpx_gt_i32_e32 17, v38
	v_mov_b32_e32 v89, v248
	v_cmpx_gt_i32_e32 16, v38
	v_mov_b32_e32 v88, v248
	v_cmpx_gt_i32_e32 11, v38
	v_mov_b32_e32 v87, v248
	v_cmpx_gt_i32_e32 10, v38
	v_mov_b32_e32 v86, v248
	v_cmpx_gt_i32_e32 9, v38
	v_mov_b32_e32 v85, v248
	v_cmpx_gt_i32_e32 8, v38
	v_mov_b32_e32 v84, v248
	v_cmpx_gt_i32_e32 3, v38
	v_mov_b32_e32 v83, v248
	v_cmpx_gt_i32_e32 2, v38
	v_mov_b32_e32 v82, v248
	v_cmpx_gt_i32_e32 1, v38
	v_mov_b32_e32 v81, v248
	v_cmpx_gt_i32_e32 0, v38
	v_mov_b32_e32 v80, v248

.LBB0_498:
	v_add_u32_e32 v182, s68, v230
	ds_read_b64_tr_b16 v[192:193], v182 offset:24576
	ds_read_b64_tr_b16 v[194:195], v182 offset:25088
	s_waitcnt lgkmcnt(9)
	v_mfma_f32_32x32x16_f16 v[48:63], v[176:179], v[128:131], v[48:63]
	v_add_f32_e32 v132, v80, v81
	v_add_f32_e32 v245, v82, v83
	v_add_f32_e32 v132, v84, v132
	v_add_f32_e32 v245, v85, v245
	v_cvt_pk_f16_f32 v144, v80, v81
	v_cvt_pk_f16_f32 v145, v82, v83
	ds_read_b64_tr_b16 v[176:177], v182 offset:28672
	ds_read_b64_tr_b16 v[178:179], v182 offset:29184
	s_waitcnt lgkmcnt(10)
	v_mfma_f32_32x32x16_f16 v[32:47], v[172:175], v[128:131], v[32:47]
	v_add_f32_e32 v80, v86, v132
	v_add_f32_e32 v245, v87, v245
	v_add_f32_e32 v80, v88, v80
	v_add_f32_e32 v245, v89, v245
	v_cvt_pk_f16_f32 v146, v84, v85
	v_cvt_pk_f16_f32 v147, v86, v87
	ds_read_b64_tr_b16 v[188:189], v182 offset:25600
	ds_read_b64_tr_b16 v[190:191], v182 offset:26112
	s_waitcnt lgkmcnt(11)
	v_mfma_f32_32x32x16_f16 v[48:63], v[168:171], v[124:127], v[48:63]
	v_add_f32_e32 v80, v90, v80
	v_add_f32_e32 v245, v91, v245
	v_add_f32_e32 v80, v92, v80
	v_add_f32_e32 v245, v93, v245
	v_cvt_pk_f16_f32 v140, v88, v89
	v_cvt_pk_f16_f32 v141, v90, v91
	ds_read_b64_tr_b16 v[84:85], v182 offset:29696
	ds_read_b64_tr_b16 v[86:87], v182 offset:30208
	s_waitcnt lgkmcnt(12)
	v_mfma_f32_32x32x16_f16 v[32:47], v[164:167], v[124:127], v[32:47]
	v_add_f32_e32 v80, v94, v80
	v_add_f32_e32 v245, v95, v245
	v_add_f32_e32 v80, v64, v80
	v_add_f32_e32 v88, v65, v80
	v_cvt_pk_f16_f32 v142, v92, v93
	v_cvt_pk_f16_f32 v143, v94, v95
	ds_read_b64_tr_b16 v[80:81], v182 offset:26624
	ds_read_b64_tr_b16 v[82:83], v182 offset:27136
	s_waitcnt lgkmcnt(13)
	v_mfma_f32_32x32x16_f16 v[48:63], v[160:163], v[120:123], v[48:63]
	v_add_f32_e32 v245, v66, v245
	v_add_f32_e32 v88, v67, v88
	v_add_f32_e32 v245, v68, v245
	v_add_f32_e32 v88, v69, v88
	v_cvt_pk_f16_f32 v136, v64, v65
	v_cvt_pk_f16_f32 v137, v66, v67
	ds_read_b64_tr_b16 v[184:185], v182 offset:30720
	ds_read_b64_tr_b16 v[186:187], v182 offset:31232
	s_waitcnt lgkmcnt(14)
	v_mfma_f32_32x32x16_f16 v[32:47], v[152:155], v[120:123], v[32:47]
	v_add_f32_e32 v64, v70, v88
	v_add_f32_e32 v245, v71, v245
	v_add_f32_e32 v64, v72, v64
	v_add_f32_e32 v88, v73, v64
	v_cvt_pk_f16_f32 v138, v68, v69
	v_cvt_pk_f16_f32 v139, v70, v71
	ds_read_b64_tr_b16 v[64:65], v182 offset:27648
	ds_read_b64_tr_b16 v[66:67], v182 offset:28160
	s_waitcnt lgkmcnt(14)
	v_mfma_f32_32x32x16_f16 v[48:63], v[156:159], v[116:119], v[48:63]
	v_add_f32_e32 v68, v74, v88
	v_add_f32_e32 v245, v75, v245
	v_add_f32_e32 v68, v76, v68
	v_add_f32_e32 v245, v77, v245
	v_cvt_pk_f16_f32 v132, v72, v73
	v_cvt_pk_f16_f32 v133, v74, v75
	ds_read_b64_tr_b16 v[180:181], v182 offset:31744
	ds_read_b64_tr_b16 v[182:183], v182 offset:32256
	v_mfma_f32_32x32x16_f16 v[32:47], v[148:151], v[116:119], v[32:47]
	v_add_f32_e32 v68, v78, v68
	v_add_f32_e32 v245, v79, v245
	v_add_f32_e32 v69, v245, v68
	v_cvt_pk_f16_f32 v134, v76, v77
	v_cvt_pk_f16_f32 v135, v78, v79
	s_add_i32 s0, s19, 3
	s_cmp_ge_u32 s0, s37
	s_cselect_b64 s[46:47], -1, 0
	s_and_b64 vcc, exec, s[46:47]
	s_cbranch_vccnz .LBB0_500
	v_lshl_add_u64 v[70:71], v[220:221], 0, s[22:23]
	s_add_i32 s0, s45, s89
	s_mov_b32 s1, m0
	s_mov_b32 m0, s0
	s_nop 0
	global_load_lds_dwordx4 v[70:71], off
	s_mov_b32 m0, s1

.LBB0_507:
	v_add_u32_e32 v182, s45, v230
	ds_read_b64_tr_b16 v[208:209], v182 offset:24576
	ds_read_b64_tr_b16 v[210:211], v182 offset:25088
	v_mfma_f32_32x32x16_f16 v[80:95], v[176:179], v[128:131], v[80:95]
	v_add_f32_e32 v132, v48, v49
	v_add_f32_e32 v245, v50, v51
	v_add_f32_e32 v132, v52, v132
	v_add_f32_e32 v245, v53, v245
	v_cvt_pk_f16_f32 v144, v48, v49
	v_cvt_pk_f16_f32 v145, v50, v51
	ds_read_b64_tr_b16 v[204:205], v182 offset:28672
	ds_read_b64_tr_b16 v[206:207], v182 offset:29184
	v_mfma_f32_32x32x16_f16 v[64:79], v[172:175], v[128:131], v[64:79]
	v_add_f32_e32 v132, v54, v132
	v_add_f32_e32 v245, v55, v245
	v_add_f32_e32 v132, v56, v132
	v_add_f32_e32 v245, v57, v245
	v_cvt_pk_f16_f32 v146, v52, v53
	v_cvt_pk_f16_f32 v147, v54, v55
	ds_read_b64_tr_b16 v[200:201], v182 offset:25600
	ds_read_b64_tr_b16 v[202:203], v182 offset:26112
	v_mfma_f32_32x32x16_f16 v[80:95], v[168:171], v[124:127], v[80:95]
	v_add_f32_e32 v132, v58, v132
	v_add_f32_e32 v245, v59, v245
	v_add_f32_e32 v132, v60, v132
	v_add_f32_e32 v245, v61, v245
	v_cvt_pk_f16_f32 v140, v56, v57
	v_cvt_pk_f16_f32 v141, v58, v59
	ds_read_b64_tr_b16 v[196:197], v182 offset:29696
	ds_read_b64_tr_b16 v[198:199], v182 offset:30208
	v_mfma_f32_32x32x16_f16 v[64:79], v[164:167], v[124:127], v[64:79]
	v_add_f32_e32 v132, v62, v132
	v_add_f32_e32 v245, v63, v245
	v_add_f32_e32 v132, v32, v132
	v_add_f32_e32 v245, v33, v245
	v_cvt_pk_f16_f32 v142, v60, v61
	v_cvt_pk_f16_f32 v143, v62, v63
	ds_read_b64_tr_b16 v[192:193], v182 offset:26624
	ds_read_b64_tr_b16 v[194:195], v182 offset:27136
	s_waitcnt lgkmcnt(13)
	v_mfma_f32_32x32x16_f16 v[80:95], v[160:163], v[120:123], v[80:95]
	v_add_f32_e32 v132, v34, v132
	v_add_f32_e32 v245, v35, v245
	v_add_f32_e32 v132, v36, v132
	v_add_f32_e32 v245, v37, v245
	v_cvt_pk_f16_f32 v136, v32, v33
	v_cvt_pk_f16_f32 v137, v34, v35
	ds_read_b64_tr_b16 v[188:189], v182 offset:30720
	ds_read_b64_tr_b16 v[190:191], v182 offset:31232
	s_waitcnt lgkmcnt(14)
	v_mfma_f32_32x32x16_f16 v[64:79], v[152:155], v[120:123], v[64:79]
	v_add_f32_e32 v132, v38, v132
	v_add_f32_e32 v245, v39, v245
	v_add_f32_e32 v132, v40, v132
	v_add_f32_e32 v245, v41, v245
	v_cvt_pk_f16_f32 v138, v36, v37
	v_cvt_pk_f16_f32 v139, v38, v39
	ds_read_b64_tr_b16 v[184:185], v182 offset:27648
	ds_read_b64_tr_b16 v[186:187], v182 offset:28160
	s_waitcnt lgkmcnt(14)
	v_mfma_f32_32x32x16_f16 v[80:95], v[156:159], v[116:119], v[80:95]
	v_add_f32_e32 v132, v42, v132
	v_add_f32_e32 v245, v43, v245
	v_add_f32_e32 v132, v44, v132
	v_add_f32_e32 v238, v45, v132
	v_cvt_pk_f16_f32 v132, v40, v41
	v_cvt_pk_f16_f32 v133, v42, v43
	ds_read_b64_tr_b16 v[180:181], v182 offset:31744
	ds_read_b64_tr_b16 v[182:183], v182 offset:32256
	v_mfma_f32_32x32x16_f16 v[64:79], v[148:151], v[116:119], v[64:79]
	v_add_f32_e32 v134, v46, v238
	v_add_f32_e32 v245, v47, v245
	v_add_f32_e32 v239, v245, v134
	v_cvt_pk_f16_f32 v134, v44, v45
	v_cvt_pk_f16_f32 v135, v46, v47
	s_add_i32 s0, s19, 4
	s_cmp_ge_u32 s0, s37
	s_cselect_b64 s[50:51], -1, 0
	s_and_b64 vcc, exec, s[50:51]
	s_cbranch_vccnz .LBB0_509
	s_add_i32 s0, s18, s89
	s_mov_b32 s1, m0
	s_mov_b32 m0, s0
	s_nop 0
	global_load_lds_dwordx4 v[220:221], off
	s_mov_b32 m0, s1

; __device__ __forceinline__ void cmask(f32x16& p0, f32x16& p1, int jb, int qrel, int hi) {
;     const float NEG = -INFINITY; int kb = 64 * jb + 4 * hi;
; #pragma unroll
;     for (int r = 0; r < 16; ++r) { int kv = kb + (r & 3) + 8 * (r >> 2); if (kv > qrel) p0[r] = NEG; if (kv + 32 > qrel) p1[r] = NEG; }
; }
.LBB0_565:
	v_add_u32_e32 v184, s18, v230
	ds_read_b64_tr_b16 v[180:181], v184 offset:24576
	ds_read_b64_tr_b16 v[182:183], v184 offset:25088
	s_waitcnt lgkmcnt(9)
	v_mfma_f32_32x32x16_f16 v[48:63], v[176:179], v[128:131], v[48:63]
	v_add_f32_e32 v132, v80, v81
	v_add_f32_e32 v245, v82, v83
	v_add_f32_e32 v132, v84, v132
	v_add_f32_e32 v245, v85, v245
	v_cvt_pk_f16_f32 v144, v80, v81
	v_cvt_pk_f16_f32 v145, v82, v83
	ds_read_b64_tr_b16 v[80:81], v184 offset:28672
	ds_read_b64_tr_b16 v[82:83], v184 offset:29184
	s_waitcnt lgkmcnt(10)
	v_mfma_f32_32x32x16_f16 v[32:47], v[172:175], v[128:131], v[32:47]
	v_add_f32_e32 v128, v86, v132
	v_add_f32_e32 v245, v87, v245
	v_add_f32_e32 v128, v88, v128
	v_add_f32_e32 v245, v89, v245
	v_cvt_pk_f16_f32 v146, v84, v85
	v_cvt_pk_f16_f32 v147, v86, v87
	ds_read_b64_tr_b16 v[84:85], v184 offset:25600
	ds_read_b64_tr_b16 v[86:87], v184 offset:26112
	s_waitcnt lgkmcnt(11)
	v_mfma_f32_32x32x16_f16 v[48:63], v[168:171], v[124:127], v[48:63]
	v_add_f32_e32 v128, v90, v128
	v_add_f32_e32 v245, v91, v245
	v_add_f32_e32 v128, v92, v128
	v_add_f32_e32 v245, v93, v245
	v_cvt_pk_f16_f32 v140, v88, v89
	v_cvt_pk_f16_f32 v141, v90, v91
	ds_read_b64_tr_b16 v[88:89], v184 offset:29696
	ds_read_b64_tr_b16 v[90:91], v184 offset:30208
	s_waitcnt lgkmcnt(12)
	v_mfma_f32_32x32x16_f16 v[32:47], v[164:167], v[124:127], v[32:47]
	v_add_f32_e32 v124, v94, v128
	v_add_f32_e32 v245, v95, v245
	v_add_f32_e32 v124, v64, v124
	v_add_f32_e32 v245, v65, v245
	v_cvt_pk_f16_f32 v142, v92, v93
	v_cvt_pk_f16_f32 v143, v94, v95
	ds_read_b64_tr_b16 v[92:93], v184 offset:26624
	ds_read_b64_tr_b16 v[94:95], v184 offset:27136
	s_waitcnt lgkmcnt(13)
	v_mfma_f32_32x32x16_f16 v[48:63], v[160:163], v[120:123], v[48:63]
	v_add_f32_e32 v124, v66, v124
	v_add_f32_e32 v245, v67, v245
	v_add_f32_e32 v124, v68, v124
	v_add_f32_e32 v245, v69, v245
	v_cvt_pk_f16_f32 v136, v64, v65
	v_cvt_pk_f16_f32 v137, v66, v67
	ds_read_b64_tr_b16 v[64:65], v184 offset:30720
	ds_read_b64_tr_b16 v[66:67], v184 offset:31232
	s_waitcnt lgkmcnt(14)
	v_mfma_f32_32x32x16_f16 v[32:47], v[152:155], v[120:123], v[32:47]
	v_add_f32_e32 v120, v70, v124
	v_add_f32_e32 v245, v71, v245
	v_add_f32_e32 v120, v72, v120
	v_add_f32_e32 v245, v73, v245
	v_cvt_pk_f16_f32 v138, v68, v69
	v_cvt_pk_f16_f32 v139, v70, v71
	ds_read_b64_tr_b16 v[68:69], v184 offset:27648
	ds_read_b64_tr_b16 v[70:71], v184 offset:28160
	s_waitcnt lgkmcnt(14)
	v_mfma_f32_32x32x16_f16 v[48:63], v[156:159], v[116:119], v[48:63]
	v_add_f32_e32 v120, v74, v120
	v_add_f32_e32 v245, v75, v245
	v_add_f32_e32 v120, v76, v120
	v_add_f32_e32 v245, v77, v245
	v_cvt_pk_f16_f32 v132, v72, v73
	v_cvt_pk_f16_f32 v133, v74, v75
	ds_read_b64_tr_b16 v[72:73], v184 offset:31744
	ds_read_b64_tr_b16 v[74:75], v184 offset:32256
	v_mfma_f32_32x32x16_f16 v[32:47], v[148:151], v[116:119], v[32:47]
	v_add_f32_e32 v116, v78, v120
	v_add_f32_e32 v245, v79, v245
	v_add_f32_e32 v116, v245, v116
	v_cvt_pk_f16_f32 v134, v76, v77
	v_cvt_pk_f16_f32 v135, v78, v79
	s_andn2_b64 vcc, exec, s[42:43]
	s_cbranch_vccnz .LBB0_567
	s_mov_b64 s[100:101], exec
	v_sub_u32_e32 v77, v215, v233
	v_add_u32_e32 v77, 0xffffff40, v77
	v_cmpx_gt_i32_e32 59, v77
	s_nop 3
	s_cbranch_execz .Lmaskx_done_5
	v_mov_b32_e32 v47, v248
	v_cmpx_gt_i32_e32 58, v77
	v_mov_b32_e32 v46, v248
	v_cmpx_gt_i32_e32 57, v77
	v_mov_b32_e32 v45, v248
	v_cmpx_gt_i32_e32 56, v77
	v_mov_b32_e32 v44, v248
	v_cmpx_gt_i32_e32 51, v77
	v_mov_b32_e32 v43, v248
	v_cmpx_gt_i32_e32 50, v77
	v_mov_b32_e32 v42, v248
	v_cmpx_gt_i32_e32 49, v77
	v_mov_b32_e32 v41, v248
	v_cmpx_gt_i32_e32 48, v77
	v_mov_b32_e32 v40, v248
	v_cmpx_gt_i32_e32 43, v77
	v_mov_b32_e32 v39, v248
	v_cmpx_gt_i32_e32 42, v77
	v_mov_b32_e32 v38, v248
	v_cmpx_gt_i32_e32 41, v77
	v_mov_b32_e32 v37, v248
	v_cmpx_gt_i32_e32 40, v77
	v_mov_b32_e32 v36, v248
	v_cmpx_gt_i32_e32 35, v77
	v_mov_b32_e32 v35, v248
	v_cmpx_gt_i32_e32 34, v77
	v_mov_b32_e32 v34, v248
	v_cmpx_gt_i32_e32 33, v77
	v_mov_b32_e32 v33, v248
	v_cmpx_gt_i32_e32 32, v77
	v_mov_b32_e32 v32, v248
	v_cmpx_gt_i32_e32 27, v77
	v_mov_b32_e32 v63, v248
	v_cmpx_gt_i32_e32 26, v77
	v_mov_b32_e32 v62, v248
	v_cmpx_gt_i32_e32 25, v77
	v_mov_b32_e32 v61, v248
	v_cmpx_gt_i32_e32 24, v77
	v_mov_b32_e32 v60, v248
	v_cmpx_gt_i32_e32 19, v77
	v_mov_b32_e32 v59, v248
	v_cmpx_gt_i32_e32 18, v77
	v_mov_b32_e32 v58, v248
	v_cmpx_gt_i32_e32 17, v77
	v_mov_b32_e32 v57, v248
	v_cmpx_gt_i32_e32 16, v77
	v_mov_b32_e32 v56, v248
	v_cmpx_gt_i32_e32 11, v77
	v_mov_b32_e32 v55, v248
	v_cmpx_gt_i32_e32 10, v77
	v_mov_b32_e32 v54, v248
	v_cmpx_gt_i32_e32 9, v77
	v_mov_b32_e32 v53, v248
	v_cmpx_gt_i32_e32 8, v77
	v_mov_b32_e32 v52, v248
	v_cmpx_gt_i32_e32 3, v77
	v_mov_b32_e32 v51, v248
	v_cmpx_gt_i32_e32 2, v77
	v_mov_b32_e32 v50, v248
	v_cmpx_gt_i32_e32 1, v77
	v_mov_b32_e32 v49, v248
	v_cmpx_gt_i32_e32 0, v77
	v_mov_b32_e32 v48, v248

; __device__ __forceinline__ void cmask(f32x16& p0, f32x16& p1, int jb, int qrel, int hi) {
;     const float NEG = -INFINITY; int kb = 64 * jb + 4 * hi;
; #pragma unroll
;     for (int r = 0; r < 16; ++r) { int kv = kb + (r & 3) + 8 * (r >> 2); if (kv > qrel) p0[r] = NEG; if (kv + 32 > qrel) p1[r] = NEG; }
; }
.LBB0_625:
	v_add_u32_e32 v184, s40, v229
	ds_read_b64_tr_b16 v[180:181], v184 offset:24576
	ds_read_b64_tr_b16 v[182:183], v184 offset:25088
	s_waitcnt lgkmcnt(9)
	v_mfma_f32_32x32x16_f16 v[48:63], v[176:179], v[128:131], v[48:63]
	v_add_f32_e32 v132, v80, v81
	v_add_f32_e32 v245, v82, v83
	v_add_f32_e32 v132, v84, v132
	v_add_f32_e32 v245, v85, v245
	v_cvt_pk_f16_f32 v144, v80, v81
	v_cvt_pk_f16_f32 v145, v82, v83
	ds_read_b64_tr_b16 v[176:177], v184 offset:28672
	ds_read_b64_tr_b16 v[178:179], v184 offset:29184
	s_waitcnt lgkmcnt(10)
	v_mfma_f32_32x32x16_f16 v[32:47], v[172:175], v[128:131], v[32:47]
	v_add_f32_e32 v80, v86, v132
	v_add_f32_e32 v245, v87, v245
	v_add_f32_e32 v80, v88, v80
	v_add_f32_e32 v245, v89, v245
	v_cvt_pk_f16_f32 v146, v84, v85
	v_cvt_pk_f16_f32 v147, v86, v87
	ds_read_b64_tr_b16 v[172:173], v184 offset:25600
	ds_read_b64_tr_b16 v[174:175], v184 offset:26112
	s_waitcnt lgkmcnt(11)
	v_mfma_f32_32x32x16_f16 v[48:63], v[168:171], v[124:127], v[48:63]
	v_add_f32_e32 v80, v90, v80
	v_add_f32_e32 v245, v91, v245
	v_add_f32_e32 v80, v92, v80
	v_add_f32_e32 v245, v93, v245
	v_cvt_pk_f16_f32 v140, v88, v89
	v_cvt_pk_f16_f32 v141, v90, v91
	ds_read_b64_tr_b16 v[84:85], v184 offset:29696
	ds_read_b64_tr_b16 v[86:87], v184 offset:30208
	s_waitcnt lgkmcnt(12)
	v_mfma_f32_32x32x16_f16 v[32:47], v[164:167], v[124:127], v[32:47]
	v_add_f32_e32 v80, v94, v80
	v_add_f32_e32 v245, v95, v245
	v_add_f32_e32 v80, v64, v80
	v_add_f32_e32 v88, v65, v80
	v_cvt_pk_f16_f32 v142, v92, v93
	v_cvt_pk_f16_f32 v143, v94, v95
	ds_read_b64_tr_b16 v[80:81], v184 offset:26624
	ds_read_b64_tr_b16 v[82:83], v184 offset:27136
	s_waitcnt lgkmcnt(13)
	v_mfma_f32_32x32x16_f16 v[48:63], v[160:163], v[120:123], v[48:63]
	v_add_f32_e32 v245, v66, v245
	v_add_f32_e32 v88, v67, v88
	v_add_f32_e32 v245, v68, v245
	v_add_f32_e32 v88, v69, v88
	v_cvt_pk_f16_f32 v136, v64, v65
	v_cvt_pk_f16_f32 v137, v66, v67
	ds_read_b64_tr_b16 v[160:161], v184 offset:30720
	ds_read_b64_tr_b16 v[162:163], v184 offset:31232
	s_waitcnt lgkmcnt(14)
	v_mfma_f32_32x32x16_f16 v[32:47], v[152:155], v[120:123], v[32:47]
	v_add_f32_e32 v64, v70, v88
	v_add_f32_e32 v245, v71, v245
	v_add_f32_e32 v64, v72, v64
	v_add_f32_e32 v88, v73, v64
	v_cvt_pk_f16_f32 v138, v68, v69
	v_cvt_pk_f16_f32 v139, v70, v71
	ds_read_b64_tr_b16 v[64:65], v184 offset:27648
	ds_read_b64_tr_b16 v[66:67], v184 offset:28160
	s_waitcnt lgkmcnt(14)
	v_mfma_f32_32x32x16_f16 v[48:63], v[156:159], v[116:119], v[48:63]
	v_add_f32_e32 v68, v74, v88
	v_add_f32_e32 v245, v75, v245
	v_add_f32_e32 v68, v76, v68
	v_add_f32_e32 v245, v77, v245
	v_cvt_pk_f16_f32 v132, v72, v73
	v_cvt_pk_f16_f32 v133, v74, v75
	ds_read_b64_tr_b16 v[152:153], v184 offset:31744
	ds_read_b64_tr_b16 v[154:155], v184 offset:32256
	v_mfma_f32_32x32x16_f16 v[32:47], v[148:151], v[116:119], v[32:47]
	v_add_f32_e32 v68, v78, v68
	v_add_f32_e32 v245, v79, v245
	v_add_f32_e32 v68, v245, v68
	v_cvt_pk_f16_f32 v134, v76, v77
	v_cvt_pk_f16_f32 v135, v78, v79
	v_lshl_add_u64 v[70:71], v[194:195], 0, s[30:31]
	s_add_i32 s11, s69, s90
	s_mov_b32 s18, m0
	s_mov_b32 m0, s11
	s_nop 0
	global_load_lds_dwordx4 v[70:71], off
	s_mov_b32 m0, s18
	s_add_i32 s18, s26, s45
	s_add_i32 s37, s26, s19
	s_add_i32 s11, s18, 1
	s_add_i32 s66, s37, 1
	s_cmp_lt_u32 s45, 3
	s_cselect_b64 s[40:41], -1, 0
	s_and_b64 s[50:51], s[40:41], exec
	s_cselect_b32 s11, s11, s66
	v_mad_i64_i32 v[70:71], s[50:51], s11, v249, v[216:217]
	s_add_i32 s50, s68, s10
	s_mov_b32 s51, m0
	s_mov_b32 m0, s50
	s_nop 0
	global_load_lds_dwordx4 v[70:71], off
	s_mov_b32 m0, s51
	s_cmp_gt_u32 s45, 3
	s_cbranch_scc1 .LBB0_627
	s_mov_b64 s[100:101], exec
	v_sub_u32_e32 v69, v215, v196
	v_add_u32_e32 v69, 32, v69
	v_cmpx_gt_i32_e32 59, v69
	s_nop 3
	s_cbranch_execz .Lmaskx_done_4
	v_mov_b32_e32 v47, v248
	v_cmpx_gt_i32_e32 58, v69
	v_mov_b32_e32 v46, v248
	v_cmpx_gt_i32_e32 57, v69
	v_mov_b32_e32 v45, v248
	v_cmpx_gt_i32_e32 56, v69
	v_mov_b32_e32 v44, v248
	v_cmpx_gt_i32_e32 51, v69
	v_mov_b32_e32 v43, v248
	v_cmpx_gt_i32_e32 50, v69
	v_mov_b32_e32 v42, v248
	v_cmpx_gt_i32_e32 49, v69
	v_mov_b32_e32 v41, v248
	v_cmpx_gt_i32_e32 48, v69
	v_mov_b32_e32 v40, v248
	v_cmpx_gt_i32_e32 43, v69
	v_mov_b32_e32 v39, v248
	v_cmpx_gt_i32_e32 42, v69
	v_mov_b32_e32 v38, v248
	v_cmpx_gt_i32_e32 41, v69
	v_mov_b32_e32 v37, v248
	v_cmpx_gt_i32_e32 40, v69
	v_mov_b32_e32 v36, v248
	v_cmpx_gt_i32_e32 35, v69
	v_mov_b32_e32 v35, v248
	v_cmpx_gt_i32_e32 34, v69
	v_mov_b32_e32 v34, v248
	v_cmpx_gt_i32_e32 33, v69
	v_mov_b32_e32 v33, v248
	v_cmpx_gt_i32_e32 32, v69
	v_mov_b32_e32 v32, v248
	v_cmpx_gt_i32_e32 27, v69
	v_mov_b32_e32 v63, v248
	v_cmpx_gt_i32_e32 26, v69
	v_mov_b32_e32 v62, v248
	v_cmpx_gt_i32_e32 25, v69
	v_mov_b32_e32 v61, v248
	v_cmpx_gt_i32_e32 24, v69
	v_mov_b32_e32 v60, v248
	v_cmpx_gt_i32_e32 19, v69
	v_mov_b32_e32 v59, v248
	v_cmpx_gt_i32_e32 18, v69
	v_mov_b32_e32 v58, v248
	v_cmpx_gt_i32_e32 17, v69
	v_mov_b32_e32 v57, v248
	v_cmpx_gt_i32_e32 16, v69
	v_mov_b32_e32 v56, v248
	v_cmpx_gt_i32_e32 11, v69
	v_mov_b32_e32 v55, v248
	v_cmpx_gt_i32_e32 10, v69
	v_mov_b32_e32 v54, v248
	v_cmpx_gt_i32_e32 9, v69
	v_mov_b32_e32 v53, v248
	v_cmpx_gt_i32_e32 8, v69
	v_mov_b32_e32 v52, v248
	v_cmpx_gt_i32_e32 3, v69
	v_mov_b32_e32 v51, v248
	v_cmpx_gt_i32_e32 2, v69
	v_mov_b32_e32 v50, v248
	v_cmpx_gt_i32_e32 1, v69
	v_mov_b32_e32 v49, v248
	v_cmpx_gt_i32_e32 0, v69
	v_mov_b32_e32 v48, v248

; __device__ __forceinline__ void cmask(f32x16& p0, f32x16& p1, int jb, int qrel, int hi) {
;     const float NEG = -INFINITY; int kb = 64 * jb + 4 * hi;
; #pragma unroll
;     for (int r = 0; r < 16; ++r) { int kv = kb + (r & 3) + 8 * (r >> 2); if (kv > qrel) p0[r] = NEG; if (kv + 32 > qrel) p1[r] = NEG; }
; }
.LBB0_630:
	s_add_i32 s11, s68, 0x2000
	s_cmpk_lg_i32 s68, 0x4000
	s_cselect_b32 s11, s11, 0
	v_add_u32_e32 v160, s69, v229
	ds_read_b64_tr_b16 v[156:157], v160 offset:24576
	ds_read_b64_tr_b16 v[158:159], v160 offset:25088
	v_mfma_f32_32x32x16_f16 v[80:95], v[188:191], v[128:131], v[80:95]
	v_add_f32_e32 v132, v48, v49
	v_add_f32_e32 v245, v50, v51
	v_add_f32_e32 v132, v52, v132
	v_add_f32_e32 v245, v53, v245
	v_cvt_pk_f16_f32 v144, v48, v49
	v_cvt_pk_f16_f32 v145, v50, v51
	ds_read_b64_tr_b16 v[152:153], v160 offset:28672
	ds_read_b64_tr_b16 v[154:155], v160 offset:29184
	v_mfma_f32_32x32x16_f16 v[64:79], v[148:151], v[128:131], v[64:79]
	v_add_f32_e32 v48, v54, v132
	v_add_f32_e32 v245, v55, v245
	v_add_f32_e32 v48, v56, v48
	v_add_f32_e32 v245, v57, v245
	v_cvt_pk_f16_f32 v146, v52, v53
	v_cvt_pk_f16_f32 v147, v54, v55
	ds_read_b64_tr_b16 v[148:149], v160 offset:25600
	ds_read_b64_tr_b16 v[150:151], v160 offset:26112
	v_mfma_f32_32x32x16_f16 v[80:95], v[184:187], v[124:127], v[80:95]
	v_add_f32_e32 v48, v58, v48
	v_add_f32_e32 v245, v59, v245
	v_add_f32_e32 v48, v60, v48
	v_add_f32_e32 v245, v61, v245
	v_cvt_pk_f16_f32 v140, v56, v57
	v_cvt_pk_f16_f32 v141, v58, v59
	ds_read_b64_tr_b16 v[52:53], v160 offset:29696
	ds_read_b64_tr_b16 v[54:55], v160 offset:30208
	v_mfma_f32_32x32x16_f16 v[64:79], v[172:175], v[124:127], v[64:79]
	v_add_f32_e32 v48, v62, v48
	v_add_f32_e32 v245, v63, v245
	v_add_f32_e32 v48, v32, v48
	v_add_f32_e32 v56, v33, v48
	v_cvt_pk_f16_f32 v142, v60, v61
	v_cvt_pk_f16_f32 v143, v62, v63
	ds_read_b64_tr_b16 v[48:49], v160 offset:26624
	ds_read_b64_tr_b16 v[50:51], v160 offset:27136
	s_waitcnt lgkmcnt(13)
	v_mfma_f32_32x32x16_f16 v[80:95], v[176:179], v[120:123], v[80:95]
	v_add_f32_e32 v245, v34, v245
	v_add_f32_e32 v56, v35, v56
	v_add_f32_e32 v245, v36, v245
	v_add_f32_e32 v56, v37, v56
	v_cvt_pk_f16_f32 v136, v32, v33
	v_cvt_pk_f16_f32 v137, v34, v35
	ds_read_b64_tr_b16 v[184:185], v160 offset:30720
	ds_read_b64_tr_b16 v[186:187], v160 offset:31232
	s_waitcnt lgkmcnt(14)
	v_mfma_f32_32x32x16_f16 v[64:79], v[164:167], v[120:123], v[64:79]
	v_add_f32_e32 v32, v38, v56
	v_add_f32_e32 v245, v39, v245
	v_add_f32_e32 v32, v40, v32
	v_add_f32_e32 v56, v41, v32
	v_cvt_pk_f16_f32 v138, v36, v37
	v_cvt_pk_f16_f32 v139, v38, v39
	ds_read_b64_tr_b16 v[32:33], v160 offset:27648
	ds_read_b64_tr_b16 v[34:35], v160 offset:28160
	s_waitcnt lgkmcnt(14)
	v_mfma_f32_32x32x16_f16 v[80:95], v[180:183], v[116:119], v[80:95]
	v_add_f32_e32 v36, v42, v56
	v_add_f32_e32 v245, v43, v245
	v_add_f32_e32 v36, v44, v36
	v_add_f32_e32 v245, v45, v245
	v_cvt_pk_f16_f32 v132, v40, v41
	v_cvt_pk_f16_f32 v133, v42, v43
	ds_read_b64_tr_b16 v[180:181], v160 offset:31744
	ds_read_b64_tr_b16 v[182:183], v160 offset:32256
	v_mfma_f32_32x32x16_f16 v[64:79], v[168:171], v[116:119], v[64:79]
	v_add_f32_e32 v36, v46, v36
	v_add_f32_e32 v245, v47, v245
	v_add_f32_e32 v36, v245, v36
	v_cvt_pk_f16_f32 v134, v44, v45
	v_cvt_pk_f16_f32 v135, v46, v47
	s_add_i32 s50, s68, s90
	s_add_i32 s18, s18, 2
	s_cmp_lt_u32 s45, 2
	s_mov_b32 s51, m0
	s_mov_b32 m0, s50
	s_nop 0
	global_load_lds_dwordx4 v[194:195], off
	s_mov_b32 m0, s51
	s_cselect_b32 s18, s18, s37
	v_mad_i64_i32 v[38:39], s[50:51], s18, v249, v[216:217]
	s_add_i32 s37, s11, s10
	s_mov_b32 s50, m0
	s_mov_b32 m0, s37
	s_nop 0
	global_load_lds_dwordx4 v[38:39], off
	s_mov_b32 m0, s50
	s_andn2_b64 vcc, exec, s[40:41]
	s_cbranch_vccnz .LBB0_632
	s_mov_b64 s[100:101], exec
	v_sub_u32_e32 v38, v215, v196
	v_add_u32_e32 v38, 0xffffffe0, v38
	v_cmpx_gt_i32_e32 59, v38
	s_nop 3
	s_cbranch_execz .Lmaskx_done_3
	v_mov_b32_e32 v79, v248
	v_cmpx_gt_i32_e32 58, v38
	v_mov_b32_e32 v78, v248
	v_cmpx_gt_i32_e32 57, v38
	v_mov_b32_e32 v77, v248
	v_cmpx_gt_i32_e32 56, v38
	v_mov_b32_e32 v76, v248
	v_cmpx_gt_i32_e32 51, v38
	v_mov_b32_e32 v75, v248
	v_cmpx_gt_i32_e32 50, v38
	v_mov_b32_e32 v74, v248
	v_cmpx_gt_i32_e32 49, v38
	v_mov_b32_e32 v73, v248
	v_cmpx_gt_i32_e32 48, v38
	v_mov_b32_e32 v72, v248
	v_cmpx_gt_i32_e32 43, v38
	v_mov_b32_e32 v71, v248
	v_cmpx_gt_i32_e32 42, v38
	v_mov_b32_e32 v70, v248
	v_cmpx_gt_i32_e32 41, v38
	v_mov_b32_e32 v69, v248
	v_cmpx_gt_i32_e32 40, v38
	v_mov_b32_e32 v68, v248
	v_cmpx_gt_i32_e32 35, v38
	v_mov_b32_e32 v67, v248
	v_cmpx_gt_i32_e32 34, v38
	v_mov_b32_e32 v66, v248
	v_cmpx_gt_i32_e32 33, v38
	v_mov_b32_e32 v65, v248
	v_cmpx_gt_i32_e32 32, v38
	v_mov_b32_e32 v64, v248
	v_cmpx_gt_i32_e32 27, v38
	v_mov_b32_e32 v95, v248
	v_cmpx_gt_i32_e32 26, v38
	v_mov_b32_e32 v94, v248
	v_cmpx_gt_i32_e32 25, v38
	v_mov_b32_e32 v93, v248
	v_cmpx_gt_i32_e32 24, v38
	v_mov_b32_e32 v92, v248
	v_cmpx_gt_i32_e32 19, v38
	v_mov_b32_e32 v91, v248
	v_cmpx_gt_i32_e32 18, v38
	v_mov_b32_e32 v90, v248
	v_cmpx_gt_i32_e32 17, v38
	v_mov_b32_e32 v89, v248
	v_cmpx_gt_i32_e32 16, v38
	v_mov_b32_e32 v88, v248
	v_cmpx_gt_i32_e32 11, v38
	v_mov_b32_e32 v87, v248
	v_cmpx_gt_i32_e32 10, v38
	v_mov_b32_e32 v86, v248
	v_cmpx_gt_i32_e32 9, v38
	v_mov_b32_e32 v85, v248
	v_cmpx_gt_i32_e32 8, v38
	v_mov_b32_e32 v84, v248
	v_cmpx_gt_i32_e32 3, v38
	v_mov_b32_e32 v83, v248
	v_cmpx_gt_i32_e32 2, v38
	v_mov_b32_e32 v82, v248
	v_cmpx_gt_i32_e32 1, v38
	v_mov_b32_e32 v81, v248
	v_cmpx_gt_i32_e32 0, v38
	v_mov_b32_e32 v80, v248

.LBB0_646:
	v_add_u32_e32 v182, s68, v229
	ds_read_b64_tr_b16 v[192:193], v182 offset:24576
	ds_read_b64_tr_b16 v[194:195], v182 offset:25088
	s_waitcnt lgkmcnt(9)
	v_mfma_f32_32x32x16_f16 v[48:63], v[176:179], v[128:131], v[48:63]
	v_add_f32_e32 v132, v80, v81
	v_add_f32_e32 v245, v82, v83
	v_add_f32_e32 v132, v84, v132
	v_add_f32_e32 v245, v85, v245
	v_cvt_pk_f16_f32 v144, v80, v81
	v_cvt_pk_f16_f32 v145, v82, v83
	ds_read_b64_tr_b16 v[176:177], v182 offset:28672
	ds_read_b64_tr_b16 v[178:179], v182 offset:29184
	s_waitcnt lgkmcnt(10)
	v_mfma_f32_32x32x16_f16 v[32:47], v[172:175], v[128:131], v[32:47]
	v_add_f32_e32 v80, v86, v132
	v_add_f32_e32 v245, v87, v245
	v_add_f32_e32 v80, v88, v80
	v_add_f32_e32 v245, v89, v245
	v_cvt_pk_f16_f32 v146, v84, v85
	v_cvt_pk_f16_f32 v147, v86, v87
	ds_read_b64_tr_b16 v[188:189], v182 offset:25600
	ds_read_b64_tr_b16 v[190:191], v182 offset:26112
	s_waitcnt lgkmcnt(11)
	v_mfma_f32_32x32x16_f16 v[48:63], v[168:171], v[124:127], v[48:63]
	v_add_f32_e32 v80, v90, v80
	v_add_f32_e32 v245, v91, v245
	v_add_f32_e32 v80, v92, v80
	v_add_f32_e32 v245, v93, v245
	v_cvt_pk_f16_f32 v140, v88, v89
	v_cvt_pk_f16_f32 v141, v90, v91
	ds_read_b64_tr_b16 v[84:85], v182 offset:29696
	ds_read_b64_tr_b16 v[86:87], v182 offset:30208
	s_waitcnt lgkmcnt(12)
	v_mfma_f32_32x32x16_f16 v[32:47], v[164:167], v[124:127], v[32:47]
	v_add_f32_e32 v80, v94, v80
	v_add_f32_e32 v245, v95, v245
	v_add_f32_e32 v80, v64, v80
	v_add_f32_e32 v88, v65, v80
	v_cvt_pk_f16_f32 v142, v92, v93
	v_cvt_pk_f16_f32 v143, v94, v95
	ds_read_b64_tr_b16 v[80:81], v182 offset:26624
	ds_read_b64_tr_b16 v[82:83], v182 offset:27136
	s_waitcnt lgkmcnt(13)
	v_mfma_f32_32x32x16_f16 v[48:63], v[160:163], v[120:123], v[48:63]
	v_add_f32_e32 v245, v66, v245
	v_add_f32_e32 v88, v67, v88
	v_add_f32_e32 v245, v68, v245
	v_add_f32_e32 v88, v69, v88
	v_cvt_pk_f16_f32 v136, v64, v65
	v_cvt_pk_f16_f32 v137, v66, v67
	ds_read_b64_tr_b16 v[184:185], v182 offset:30720
	ds_read_b64_tr_b16 v[186:187], v182 offset:31232
	s_waitcnt lgkmcnt(14)
	v_mfma_f32_32x32x16_f16 v[32:47], v[152:155], v[120:123], v[32:47]
	v_add_f32_e32 v64, v70, v88
	v_add_f32_e32 v245, v71, v245
	v_add_f32_e32 v64, v72, v64
	v_add_f32_e32 v88, v73, v64
	v_cvt_pk_f16_f32 v138, v68, v69
	v_cvt_pk_f16_f32 v139, v70, v71
	ds_read_b64_tr_b16 v[64:65], v182 offset:27648
	ds_read_b64_tr_b16 v[66:67], v182 offset:28160
	s_waitcnt lgkmcnt(14)
	v_mfma_f32_32x32x16_f16 v[48:63], v[156:159], v[116:119], v[48:63]
	v_add_f32_e32 v68, v74, v88
	v_add_f32_e32 v245, v75, v245
	v_add_f32_e32 v68, v76, v68
	v_add_f32_e32 v245, v77, v245
	v_cvt_pk_f16_f32 v132, v72, v73
	v_cvt_pk_f16_f32 v133, v74, v75
	ds_read_b64_tr_b16 v[180:181], v182 offset:31744
	ds_read_b64_tr_b16 v[182:183], v182 offset:32256
	v_mfma_f32_32x32x16_f16 v[32:47], v[148:151], v[116:119], v[32:47]
	v_add_f32_e32 v68, v78, v68
	v_add_f32_e32 v245, v79, v245
	v_add_f32_e32 v68, v245, v68
	v_cvt_pk_f16_f32 v134, v76, v77
	v_cvt_pk_f16_f32 v135, v78, v79
	s_add_i32 s28, s37, 3
	s_cmp_ge_u32 s28, s36
	s_cselect_b64 s[50:51], -1, 0
	s_and_b64 vcc, exec, s[50:51]
	s_cbranch_vccnz .LBB0_648
	s_add_i32 s28, s11, s90
	s_mov_b32 s40, m0
	s_mov_b32 m0, s28
	s_nop 0
	global_load_lds_dwordx4 v[220:221], off
	s_mov_b32 m0, s40

.LBB0_655:
	v_add_u32_e32 v182, s11, v229
	ds_read_b64_tr_b16 v[208:209], v182 offset:24576
	ds_read_b64_tr_b16 v[210:211], v182 offset:25088
	v_mfma_f32_32x32x16_f16 v[80:95], v[176:179], v[128:131], v[80:95]
	v_add_f32_e32 v132, v48, v49
	v_add_f32_e32 v245, v50, v51
	v_add_f32_e32 v132, v52, v132
	v_add_f32_e32 v245, v53, v245
	v_cvt_pk_f16_f32 v144, v48, v49
	v_cvt_pk_f16_f32 v145, v50, v51
	ds_read_b64_tr_b16 v[204:205], v182 offset:28672
	ds_read_b64_tr_b16 v[206:207], v182 offset:29184
	v_mfma_f32_32x32x16_f16 v[64:79], v[172:175], v[128:131], v[64:79]
	v_add_f32_e32 v132, v54, v132
	v_add_f32_e32 v245, v55, v245
	v_add_f32_e32 v132, v56, v132
	v_add_f32_e32 v245, v57, v245
	v_cvt_pk_f16_f32 v146, v52, v53
	v_cvt_pk_f16_f32 v147, v54, v55
	ds_read_b64_tr_b16 v[200:201], v182 offset:25600
	ds_read_b64_tr_b16 v[202:203], v182 offset:26112
	v_mfma_f32_32x32x16_f16 v[80:95], v[168:171], v[124:127], v[80:95]
	v_add_f32_e32 v132, v58, v132
	v_add_f32_e32 v245, v59, v245
	v_add_f32_e32 v132, v60, v132
	v_add_f32_e32 v245, v61, v245
	v_cvt_pk_f16_f32 v140, v56, v57
	v_cvt_pk_f16_f32 v141, v58, v59
	ds_read_b64_tr_b16 v[196:197], v182 offset:29696
	ds_read_b64_tr_b16 v[198:199], v182 offset:30208
	v_mfma_f32_32x32x16_f16 v[64:79], v[164:167], v[124:127], v[64:79]
	v_add_f32_e32 v132, v62, v132
	v_add_f32_e32 v245, v63, v245
	v_add_f32_e32 v132, v32, v132
	v_add_f32_e32 v245, v33, v245
	v_cvt_pk_f16_f32 v142, v60, v61
	v_cvt_pk_f16_f32 v143, v62, v63
	ds_read_b64_tr_b16 v[192:193], v182 offset:26624
	ds_read_b64_tr_b16 v[194:195], v182 offset:27136
	s_waitcnt lgkmcnt(13)
	v_mfma_f32_32x32x16_f16 v[80:95], v[160:163], v[120:123], v[80:95]
	v_add_f32_e32 v132, v34, v132
	v_add_f32_e32 v245, v35, v245
	v_add_f32_e32 v132, v36, v132
	v_add_f32_e32 v245, v37, v245
	v_cvt_pk_f16_f32 v136, v32, v33
	v_cvt_pk_f16_f32 v137, v34, v35
	ds_read_b64_tr_b16 v[188:189], v182 offset:30720
	ds_read_b64_tr_b16 v[190:191], v182 offset:31232
	s_waitcnt lgkmcnt(14)
	v_mfma_f32_32x32x16_f16 v[64:79], v[152:155], v[120:123], v[64:79]
	v_add_f32_e32 v132, v38, v132
	v_add_f32_e32 v245, v39, v245
	v_add_f32_e32 v132, v40, v132
	v_add_f32_e32 v245, v41, v245
	v_cvt_pk_f16_f32 v138, v36, v37
	v_cvt_pk_f16_f32 v139, v38, v39
	ds_read_b64_tr_b16 v[184:185], v182 offset:27648
	ds_read_b64_tr_b16 v[186:187], v182 offset:28160
	s_waitcnt lgkmcnt(14)
	v_mfma_f32_32x32x16_f16 v[80:95], v[156:159], v[116:119], v[80:95]
	v_add_f32_e32 v132, v42, v132
	v_add_f32_e32 v245, v43, v245
	v_add_f32_e32 v132, v44, v132
	v_add_f32_e32 v235, v45, v132
	v_cvt_pk_f16_f32 v132, v40, v41
	v_cvt_pk_f16_f32 v133, v42, v43
	ds_read_b64_tr_b16 v[180:181], v182 offset:31744
	ds_read_b64_tr_b16 v[182:183], v182 offset:32256
	v_mfma_f32_32x32x16_f16 v[64:79], v[148:151], v[116:119], v[64:79]
	v_add_f32_e32 v134, v46, v235
	v_add_f32_e32 v245, v47, v245
	v_add_f32_e32 v235, v245, v134
	v_cvt_pk_f16_f32 v134, v44, v45
	v_cvt_pk_f16_f32 v135, v46, v47
	s_add_i32 s11, s37, 4
	s_cmp_ge_u32 s11, s36
	s_cselect_b64 s[66:67], -1, 0
	s_and_b64 vcc, exec, s[66:67]
	s_cbranch_vccnz .LBB0_657
	v_lshl_add_u64 v[236:237], v[220:221], 0, s[22:23]
	s_add_i32 s11, s18, s90
	s_mov_b32 s45, m0
	s_mov_b32 m0, s11
	s_nop 0
	global_load_lds_dwordx4 v[236:237], off
	s_mov_b32 m0, s45

; __device__ __forceinline__ void cmask(f32x16& p0, f32x16& p1, int jb, int qrel, int hi) {
;     const float NEG = -INFINITY; int kb = 64 * jb + 4 * hi;
; #pragma unroll
;     for (int r = 0; r < 16; ++r) { int kv = kb + (r & 3) + 8 * (r >> 2); if (kv > qrel) p0[r] = NEG; if (kv + 32 > qrel) p1[r] = NEG; }
; }
.LBB0_711:
	v_add_u32_e32 v184, s18, v229
	ds_read_b64_tr_b16 v[180:181], v184 offset:24576
	ds_read_b64_tr_b16 v[182:183], v184 offset:25088
	s_waitcnt lgkmcnt(9)
	v_mfma_f32_32x32x16_f16 v[48:63], v[176:179], v[128:131], v[48:63]
	v_add_f32_e32 v132, v80, v81
	v_add_f32_e32 v245, v82, v83
	v_add_f32_e32 v132, v84, v132
	v_add_f32_e32 v245, v85, v245
	v_cvt_pk_f16_f32 v144, v80, v81
	v_cvt_pk_f16_f32 v145, v82, v83
	ds_read_b64_tr_b16 v[80:81], v184 offset:28672
	ds_read_b64_tr_b16 v[82:83], v184 offset:29184
	s_waitcnt lgkmcnt(10)
	v_mfma_f32_32x32x16_f16 v[32:47], v[172:175], v[128:131], v[32:47]
	v_add_f32_e32 v128, v86, v132
	v_add_f32_e32 v245, v87, v245
	v_add_f32_e32 v128, v88, v128
	v_add_f32_e32 v245, v89, v245
	v_cvt_pk_f16_f32 v146, v84, v85
	v_cvt_pk_f16_f32 v147, v86, v87
	ds_read_b64_tr_b16 v[84:85], v184 offset:25600
	ds_read_b64_tr_b16 v[86:87], v184 offset:26112
	s_waitcnt lgkmcnt(11)
	v_mfma_f32_32x32x16_f16 v[48:63], v[168:171], v[124:127], v[48:63]
	v_add_f32_e32 v128, v90, v128
	v_add_f32_e32 v245, v91, v245
	v_add_f32_e32 v128, v92, v128
	v_add_f32_e32 v245, v93, v245
	v_cvt_pk_f16_f32 v140, v88, v89
	v_cvt_pk_f16_f32 v141, v90, v91
	ds_read_b64_tr_b16 v[88:89], v184 offset:29696
	ds_read_b64_tr_b16 v[90:91], v184 offset:30208
	s_waitcnt lgkmcnt(12)
	v_mfma_f32_32x32x16_f16 v[32:47], v[164:167], v[124:127], v[32:47]
	v_add_f32_e32 v124, v94, v128
	v_add_f32_e32 v245, v95, v245
	v_add_f32_e32 v124, v64, v124
	v_add_f32_e32 v245, v65, v245
	v_cvt_pk_f16_f32 v142, v92, v93
	v_cvt_pk_f16_f32 v143, v94, v95
	ds_read_b64_tr_b16 v[92:93], v184 offset:26624
	ds_read_b64_tr_b16 v[94:95], v184 offset:27136
	s_waitcnt lgkmcnt(13)
	v_mfma_f32_32x32x16_f16 v[48:63], v[160:163], v[120:123], v[48:63]
	v_add_f32_e32 v124, v66, v124
	v_add_f32_e32 v245, v67, v245
	v_add_f32_e32 v124, v68, v124
	v_add_f32_e32 v245, v69, v245
	v_cvt_pk_f16_f32 v136, v64, v65
	v_cvt_pk_f16_f32 v137, v66, v67
	ds_read_b64_tr_b16 v[64:65], v184 offset:30720
	ds_read_b64_tr_b16 v[66:67], v184 offset:31232
	s_waitcnt lgkmcnt(14)
	v_mfma_f32_32x32x16_f16 v[32:47], v[152:155], v[120:123], v[32:47]
	v_add_f32_e32 v120, v70, v124
	v_add_f32_e32 v245, v71, v245
	v_add_f32_e32 v120, v72, v120
	v_add_f32_e32 v245, v73, v245
	v_cvt_pk_f16_f32 v138, v68, v69
	v_cvt_pk_f16_f32 v139, v70, v71
	ds_read_b64_tr_b16 v[68:69], v184 offset:27648
	ds_read_b64_tr_b16 v[70:71], v184 offset:28160
	s_waitcnt lgkmcnt(14)
	v_mfma_f32_32x32x16_f16 v[48:63], v[156:159], v[116:119], v[48:63]
	v_add_f32_e32 v120, v74, v120
	v_add_f32_e32 v245, v75, v245
	v_add_f32_e32 v120, v76, v120
	v_add_f32_e32 v245, v77, v245
	v_cvt_pk_f16_f32 v132, v72, v73
	v_cvt_pk_f16_f32 v133, v74, v75
	ds_read_b64_tr_b16 v[72:73], v184 offset:31744
	ds_read_b64_tr_b16 v[74:75], v184 offset:32256
	v_mfma_f32_32x32x16_f16 v[32:47], v[148:151], v[116:119], v[32:47]
	v_add_f32_e32 v116, v78, v120
	v_add_f32_e32 v245, v79, v245
	v_add_f32_e32 v116, v245, v116
	v_cvt_pk_f16_f32 v134, v76, v77
	v_cvt_pk_f16_f32 v135, v78, v79
	s_andn2_b64 vcc, exec, s[0:1]
	s_cbranch_vccnz .LBB0_713
	s_mov_b64 s[100:101], exec
	v_sub_u32_e32 v77, v215, v231
	v_add_u32_e32 v77, 0xffffff40, v77
	v_cmpx_gt_i32_e32 59, v77
	s_nop 3
	s_cbranch_execz .Lmaskx_done_0
	v_mov_b32_e32 v47, v248
	v_cmpx_gt_i32_e32 58, v77
	v_mov_b32_e32 v46, v248
	v_cmpx_gt_i32_e32 57, v77
	v_mov_b32_e32 v45, v248
	v_cmpx_gt_i32_e32 56, v77
	v_mov_b32_e32 v44, v248
	v_cmpx_gt_i32_e32 51, v77
	v_mov_b32_e32 v43, v248
	v_cmpx_gt_i32_e32 50, v77
	v_mov_b32_e32 v42, v248
	v_cmpx_gt_i32_e32 49, v77
	v_mov_b32_e32 v41, v248
	v_cmpx_gt_i32_e32 48, v77
	v_mov_b32_e32 v40, v248
	v_cmpx_gt_i32_e32 43, v77
	v_mov_b32_e32 v39, v248
	v_cmpx_gt_i32_e32 42, v77
	v_mov_b32_e32 v38, v248
	v_cmpx_gt_i32_e32 41, v77
	v_mov_b32_e32 v37, v248
	v_cmpx_gt_i32_e32 40, v77
	v_mov_b32_e32 v36, v248
	v_cmpx_gt_i32_e32 35, v77
	v_mov_b32_e32 v35, v248
	v_cmpx_gt_i32_e32 34, v77
	v_mov_b32_e32 v34, v248
	v_cmpx_gt_i32_e32 33, v77
	v_mov_b32_e32 v33, v248
	v_cmpx_gt_i32_e32 32, v77
	v_mov_b32_e32 v32, v248
	v_cmpx_gt_i32_e32 27, v77
	v_mov_b32_e32 v63, v248
	v_cmpx_gt_i32_e32 26, v77
	v_mov_b32_e32 v62, v248
	v_cmpx_gt_i32_e32 25, v77
	v_mov_b32_e32 v61, v248
	v_cmpx_gt_i32_e32 24, v77
	v_mov_b32_e32 v60, v248
	v_cmpx_gt_i32_e32 19, v77
	v_mov_b32_e32 v59, v248
	v_cmpx_gt_i32_e32 18, v77
	v_mov_b32_e32 v58, v248
	v_cmpx_gt_i32_e32 17, v77
	v_mov_b32_e32 v57, v248
	v_cmpx_gt_i32_e32 16, v77
	v_mov_b32_e32 v56, v248
	v_cmpx_gt_i32_e32 11, v77
	v_mov_b32_e32 v55, v248
	v_cmpx_gt_i32_e32 10, v77
	v_mov_b32_e32 v54, v248
	v_cmpx_gt_i32_e32 9, v77
	v_mov_b32_e32 v53, v248
	v_cmpx_gt_i32_e32 8, v77
	v_mov_b32_e32 v52, v248
	v_cmpx_gt_i32_e32 3, v77
	v_mov_b32_e32 v51, v248
	v_cmpx_gt_i32_e32 2, v77
	v_mov_b32_e32 v50, v248
	v_cmpx_gt_i32_e32 1, v77
	v_mov_b32_e32 v49, v248
	v_cmpx_gt_i32_e32 0, v77
	v_mov_b32_e32 v48, v248
